# P1 fp8 gate tiles: gate-bias loads issued together without draining the DMA ring; gate epilogue waits once instead of draining each store
# baseline (speedup 1.0000x reference)
.LBB0_403:
	s_cmp_eq_u32 s68, 12
	s_cselect_b64 s[36:37], -1, 0
	s_cmp_lg_u32 s68, 12
	s_cbranch_scc1 .LBB0_402
	v_cndmask_b32_e64 v2, 0, 1, s[4:5]
	v_cmp_ne_u32_e64 s[0:1], 1, v2
	v_mov_b32_e32 v36, v34
	v_mov_b32_e32 v37, v34
	v_mov_b32_e32 v35, v34
	v_mov_b64_e32 v[250:251], v[36:37]
	v_mov_b64_e32 v[248:249], v[34:35]
	v_mov_b64_e32 v[222:223], v[36:37]
	v_mov_b64_e32 v[220:221], v[34:35]
	v_mov_b64_e32 v[48:49], v[36:37]
	v_mov_b64_e32 v[46:47], v[34:35]
	v_mov_b32_e32 v53, 0
	v_mov_b32_e32 v52, 0
	v_mov_b32_e32 v51, 0
	v_mov_b32_e32 v50, 0
	s_andn2_b64 vcc, exec, s[4:5]
	s_cbranch_vccnz .LBB0_402
	global_load_dwordx4 v[248:251], v[196:197], off
	global_load_dwordx4 v[220:223], v[198:199], off
	global_load_dwordx4 v[46:49], v[200:201], off
	global_load_dwordx4 v[50:53], v[202:203], off
	s_branch .LBB0_402

.LBB0_421:
	s_andn2_b64 vcc, exec, s[0:1]
	s_cbranch_vccnz .LBB0_423
	v_pk_add_f32 v[10:11], v[48:49], v[172:173]
	v_pk_add_f32 v[6:7], v[46:47], v[170:171]
	v_pk_add_f32 v[8:9], v[50:51], v[166:167]
	v_pk_add_f32 v[12:13], v[52:53], v[168:169]
	v_mul_f32_e32 v6, 0xbfb8aa3b, v6
	v_mul_f32_e32 v8, 0xbfb8aa3b, v8
	v_mul_f32_e32 v7, 0xbfb8aa3b, v7
	v_mul_f32_e32 v9, 0xbfb8aa3b, v9
	v_mul_f32_e32 v10, 0xbfb8aa3b, v10
	v_mul_f32_e32 v12, 0xbfb8aa3b, v12
	v_mul_f32_e32 v11, 0xbfb8aa3b, v11
	v_mul_f32_e32 v13, 0xbfb8aa3b, v13
	v_exp_f32_e32 v6, v6
	v_exp_f32_e32 v8, v8
	v_exp_f32_e32 v7, v7
	v_exp_f32_e32 v9, v9
	v_exp_f32_e32 v10, v10
	v_exp_f32_e32 v12, v12
	v_exp_f32_e32 v11, v11
	v_exp_f32_e32 v13, v13
	v_add_f32_e32 v6, 1.0, v6
	v_add_f32_e32 v8, 1.0, v8
	v_add_f32_e32 v7, 1.0, v7
	v_add_f32_e32 v9, 1.0, v9
	v_add_f32_e32 v10, 1.0, v10
	v_add_f32_e32 v12, 1.0, v12
	v_add_f32_e32 v11, 1.0, v11
	v_add_f32_e32 v13, 1.0, v13
	v_rcp_f32_e32 v6, v6
	v_rcp_f32_e32 v8, v8
	v_rcp_f32_e32 v7, v7
	v_rcp_f32_e32 v9, v9
	v_rcp_f32_e32 v10, v10
	v_rcp_f32_e32 v12, v12
	v_rcp_f32_e32 v11, v11
	v_rcp_f32_e32 v13, v13

.LBB0_425:
	s_andn2_b64 vcc, exec, s[0:1]
	s_cbranch_vccnz .LBB0_427
	v_pk_add_f32 v[4:5], v[250:251], v[164:165]
	v_pk_add_f32 v[10:11], v[222:223], v[160:161]
	v_mul_f32_e32 v4, 0xbfb8aa3b, v4
	v_exp_f32_e32 v4, v4
	v_mul_f32_e32 v10, 0xbfb8aa3b, v10
	v_pk_add_f32 v[6:7], v[248:249], v[162:163]
	v_pk_add_f32 v[8:9], v[220:221], v[158:159]
	v_exp_f32_e32 v12, v10
	v_mul_f32_e32 v5, 0xbfb8aa3b, v5
	v_mul_f32_e32 v6, 0xbfb8aa3b, v6
	v_mul_f32_e32 v8, 0xbfb8aa3b, v8
	v_mul_f32_e32 v7, 0xbfb8aa3b, v7
	v_mul_f32_e32 v9, 0xbfb8aa3b, v9
	v_exp_f32_e32 v5, v5
	v_mul_f32_e32 v11, 0xbfb8aa3b, v11
	v_exp_f32_e32 v6, v6
	v_exp_f32_e32 v8, v8
	v_exp_f32_e32 v7, v7
	v_exp_f32_e32 v9, v9
	v_exp_f32_e32 v13, v11
	v_add_f32_e32 v4, 1.0, v4
	v_rcp_f32_e32 v10, v4
	v_add_f32_e32 v4, 1.0, v12
	v_rcp_f32_e32 v12, v4
	v_add_f32_e32 v4, 1.0, v5
	v_add_f32_e32 v6, 1.0, v6
	v_add_f32_e32 v8, 1.0, v8
	v_add_f32_e32 v7, 1.0, v7
	v_add_f32_e32 v9, 1.0, v9
	v_rcp_f32_e32 v11, v4
	v_add_f32_e32 v4, 1.0, v13
	v_rcp_f32_e32 v6, v6
	v_rcp_f32_e32 v8, v8
	v_rcp_f32_e32 v7, v7
	v_rcp_f32_e32 v9, v9
	v_rcp_f32_e32 v13, v4

.LBB0_429:
	s_andn2_b64 vcc, exec, s[0:1]
	s_cbranch_vccnz .LBB0_431
	v_pk_add_f32 v[10:11], v[48:49], v[156:157]
	v_pk_add_f32 v[6:7], v[46:47], v[154:155]
	v_pk_add_f32 v[8:9], v[50:51], v[150:151]
	v_pk_add_f32 v[12:13], v[52:53], v[152:153]
	v_mul_f32_e32 v6, 0xbfb8aa3b, v6
	v_mul_f32_e32 v8, 0xbfb8aa3b, v8
	v_mul_f32_e32 v7, 0xbfb8aa3b, v7
	v_mul_f32_e32 v9, 0xbfb8aa3b, v9
	v_mul_f32_e32 v10, 0xbfb8aa3b, v10
	v_mul_f32_e32 v12, 0xbfb8aa3b, v12
	v_mul_f32_e32 v11, 0xbfb8aa3b, v11
	v_mul_f32_e32 v13, 0xbfb8aa3b, v13
	v_exp_f32_e32 v6, v6
	v_exp_f32_e32 v8, v8
	v_exp_f32_e32 v7, v7
	v_exp_f32_e32 v9, v9
	v_exp_f32_e32 v10, v10
	v_exp_f32_e32 v12, v12
	v_exp_f32_e32 v11, v11
	v_exp_f32_e32 v13, v13
	v_add_f32_e32 v6, 1.0, v6
	v_add_f32_e32 v8, 1.0, v8
	v_add_f32_e32 v7, 1.0, v7
	v_add_f32_e32 v9, 1.0, v9
	v_add_f32_e32 v10, 1.0, v10
	v_add_f32_e32 v12, 1.0, v12
	v_add_f32_e32 v11, 1.0, v11
	v_add_f32_e32 v13, 1.0, v13
	v_rcp_f32_e32 v6, v6
	v_rcp_f32_e32 v8, v8
	v_rcp_f32_e32 v7, v7
	v_rcp_f32_e32 v9, v9
	v_rcp_f32_e32 v10, v10
	v_rcp_f32_e32 v12, v12
	v_rcp_f32_e32 v11, v11
	v_rcp_f32_e32 v13, v13

.LBB0_433:
	s_andn2_b64 vcc, exec, s[0:1]
	s_cbranch_vccnz .LBB0_435
	v_pk_add_f32 v[4:5], v[250:251], v[148:149]
	v_pk_add_f32 v[10:11], v[222:223], v[144:145]
	v_mul_f32_e32 v4, 0xbfb8aa3b, v4
	v_exp_f32_e32 v4, v4
	v_mul_f32_e32 v10, 0xbfb8aa3b, v10
	v_pk_add_f32 v[6:7], v[248:249], v[146:147]
	v_pk_add_f32 v[8:9], v[220:221], v[142:143]
	v_exp_f32_e32 v12, v10
	v_mul_f32_e32 v5, 0xbfb8aa3b, v5
	v_mul_f32_e32 v6, 0xbfb8aa3b, v6
	v_mul_f32_e32 v8, 0xbfb8aa3b, v8
	v_mul_f32_e32 v7, 0xbfb8aa3b, v7
	v_mul_f32_e32 v9, 0xbfb8aa3b, v9
	v_exp_f32_e32 v5, v5
	v_mul_f32_e32 v11, 0xbfb8aa3b, v11
	v_exp_f32_e32 v6, v6
	v_exp_f32_e32 v8, v8
	v_exp_f32_e32 v7, v7
	v_exp_f32_e32 v9, v9
	v_exp_f32_e32 v13, v11
	v_add_f32_e32 v4, 1.0, v4
	v_rcp_f32_e32 v10, v4
	v_add_f32_e32 v4, 1.0, v12
	v_rcp_f32_e32 v12, v4
	v_add_f32_e32 v4, 1.0, v5
	v_add_f32_e32 v6, 1.0, v6
	v_add_f32_e32 v8, 1.0, v8
	v_add_f32_e32 v7, 1.0, v7
	v_add_f32_e32 v9, 1.0, v9
	v_rcp_f32_e32 v11, v4
	v_add_f32_e32 v4, 1.0, v13
	v_rcp_f32_e32 v6, v6
	v_rcp_f32_e32 v8, v8
	v_rcp_f32_e32 v7, v7
	v_rcp_f32_e32 v9, v9
	v_rcp_f32_e32 v13, v4

.LBB0_437:
	s_andn2_b64 vcc, exec, s[0:1]
	s_cbranch_vccnz .LBB0_439
	v_pk_add_f32 v[10:11], v[48:49], v[140:141]
	v_pk_add_f32 v[6:7], v[46:47], v[138:139]
	v_pk_add_f32 v[8:9], v[50:51], v[134:135]
	v_pk_add_f32 v[12:13], v[52:53], v[136:137]
	v_mul_f32_e32 v6, 0xbfb8aa3b, v6
	v_mul_f32_e32 v8, 0xbfb8aa3b, v8
	v_mul_f32_e32 v7, 0xbfb8aa3b, v7
	v_mul_f32_e32 v9, 0xbfb8aa3b, v9
	v_mul_f32_e32 v10, 0xbfb8aa3b, v10
	v_mul_f32_e32 v12, 0xbfb8aa3b, v12
	v_mul_f32_e32 v11, 0xbfb8aa3b, v11
	v_mul_f32_e32 v13, 0xbfb8aa3b, v13
	v_exp_f32_e32 v6, v6
	v_exp_f32_e32 v8, v8
	v_exp_f32_e32 v7, v7
	v_exp_f32_e32 v9, v9
	v_exp_f32_e32 v10, v10
	v_exp_f32_e32 v12, v12
	v_exp_f32_e32 v11, v11
	v_exp_f32_e32 v13, v13
	v_add_f32_e32 v6, 1.0, v6
	v_add_f32_e32 v8, 1.0, v8
	v_add_f32_e32 v7, 1.0, v7
	v_add_f32_e32 v9, 1.0, v9
	v_add_f32_e32 v10, 1.0, v10
	v_add_f32_e32 v12, 1.0, v12
	v_add_f32_e32 v11, 1.0, v11
	v_add_f32_e32 v13, 1.0, v13
	v_rcp_f32_e32 v6, v6
	v_rcp_f32_e32 v8, v8
	v_rcp_f32_e32 v7, v7
	v_rcp_f32_e32 v9, v9
	v_rcp_f32_e32 v10, v10
	v_rcp_f32_e32 v12, v12
	v_rcp_f32_e32 v11, v11
	v_rcp_f32_e32 v13, v13

.LBB0_441:
	s_andn2_b64 vcc, exec, s[0:1]
	s_cbranch_vccnz .LBB0_443
	v_pk_add_f32 v[4:5], v[250:251], v[132:133]
	v_pk_add_f32 v[10:11], v[222:223], v[128:129]
	v_mul_f32_e32 v4, 0xbfb8aa3b, v4
	v_exp_f32_e32 v4, v4
	v_mul_f32_e32 v10, 0xbfb8aa3b, v10
	v_pk_add_f32 v[6:7], v[248:249], v[130:131]
	v_pk_add_f32 v[8:9], v[220:221], v[126:127]
	v_exp_f32_e32 v12, v10
	v_mul_f32_e32 v5, 0xbfb8aa3b, v5
	v_mul_f32_e32 v6, 0xbfb8aa3b, v6
	v_mul_f32_e32 v8, 0xbfb8aa3b, v8
	v_mul_f32_e32 v7, 0xbfb8aa3b, v7
	v_mul_f32_e32 v9, 0xbfb8aa3b, v9
	v_exp_f32_e32 v5, v5
	v_mul_f32_e32 v11, 0xbfb8aa3b, v11
	v_exp_f32_e32 v6, v6
	v_exp_f32_e32 v8, v8
	v_exp_f32_e32 v7, v7
	v_exp_f32_e32 v9, v9
	v_exp_f32_e32 v13, v11
	v_add_f32_e32 v4, 1.0, v4
	v_rcp_f32_e32 v10, v4
	v_add_f32_e32 v4, 1.0, v12
	v_rcp_f32_e32 v12, v4
	v_add_f32_e32 v4, 1.0, v5
	v_add_f32_e32 v6, 1.0, v6
	v_add_f32_e32 v8, 1.0, v8
	v_add_f32_e32 v7, 1.0, v7
	v_add_f32_e32 v9, 1.0, v9
	v_rcp_f32_e32 v11, v4
	v_add_f32_e32 v4, 1.0, v13
	v_rcp_f32_e32 v6, v6
	v_rcp_f32_e32 v8, v8
	v_rcp_f32_e32 v7, v7
	v_rcp_f32_e32 v9, v9
	v_rcp_f32_e32 v13, v4

.LBB0_445:
	s_andn2_b64 vcc, exec, s[0:1]
	s_cbranch_vccnz .LBB0_447
	v_pk_add_f32 v[10:11], v[48:49], v[124:125]
	v_pk_add_f32 v[6:7], v[46:47], v[122:123]
	v_pk_add_f32 v[8:9], v[50:51], v[118:119]
	v_pk_add_f32 v[12:13], v[52:53], v[120:121]
	v_mul_f32_e32 v6, 0xbfb8aa3b, v6
	v_mul_f32_e32 v8, 0xbfb8aa3b, v8
	v_mul_f32_e32 v7, 0xbfb8aa3b, v7
	v_mul_f32_e32 v9, 0xbfb8aa3b, v9
	v_mul_f32_e32 v10, 0xbfb8aa3b, v10
	v_mul_f32_e32 v12, 0xbfb8aa3b, v12
	v_mul_f32_e32 v11, 0xbfb8aa3b, v11
	v_mul_f32_e32 v13, 0xbfb8aa3b, v13
	v_exp_f32_e32 v6, v6
	v_exp_f32_e32 v8, v8
	v_exp_f32_e32 v7, v7
	v_exp_f32_e32 v9, v9
	v_exp_f32_e32 v10, v10
	v_exp_f32_e32 v12, v12
	v_exp_f32_e32 v11, v11
	v_exp_f32_e32 v13, v13
	v_add_f32_e32 v6, 1.0, v6
	v_add_f32_e32 v8, 1.0, v8
	v_add_f32_e32 v7, 1.0, v7
	v_add_f32_e32 v9, 1.0, v9
	v_add_f32_e32 v10, 1.0, v10
	v_add_f32_e32 v12, 1.0, v12
	v_add_f32_e32 v11, 1.0, v11
	v_add_f32_e32 v13, 1.0, v13
	v_rcp_f32_e32 v6, v6
	v_rcp_f32_e32 v8, v8
	v_rcp_f32_e32 v7, v7
	v_rcp_f32_e32 v9, v9
	v_rcp_f32_e32 v10, v10
	v_rcp_f32_e32 v12, v12
	v_rcp_f32_e32 v11, v11
	v_rcp_f32_e32 v13, v13

.LBB0_449:
	s_andn2_b64 vcc, exec, s[0:1]
	s_cbranch_vccnz .LBB0_451
	v_pk_add_f32 v[4:5], v[250:251], v[116:117]
	v_pk_add_f32 v[10:11], v[222:223], v[112:113]
	v_mul_f32_e32 v4, 0xbfb8aa3b, v4
	v_exp_f32_e32 v4, v4
	v_mul_f32_e32 v10, 0xbfb8aa3b, v10
	v_pk_add_f32 v[6:7], v[248:249], v[114:115]
	v_pk_add_f32 v[8:9], v[220:221], v[110:111]
	v_exp_f32_e32 v12, v10
	v_mul_f32_e32 v5, 0xbfb8aa3b, v5
	v_mul_f32_e32 v6, 0xbfb8aa3b, v6
	v_mul_f32_e32 v8, 0xbfb8aa3b, v8
	v_mul_f32_e32 v7, 0xbfb8aa3b, v7
	v_mul_f32_e32 v9, 0xbfb8aa3b, v9
	v_exp_f32_e32 v5, v5
	v_mul_f32_e32 v11, 0xbfb8aa3b, v11
	v_exp_f32_e32 v6, v6
	v_exp_f32_e32 v8, v8
	v_exp_f32_e32 v7, v7
	v_exp_f32_e32 v9, v9
	v_exp_f32_e32 v13, v11
	v_add_f32_e32 v4, 1.0, v4
	v_rcp_f32_e32 v10, v4
	v_add_f32_e32 v4, 1.0, v12
	v_rcp_f32_e32 v12, v4
	v_add_f32_e32 v4, 1.0, v5
	v_add_f32_e32 v6, 1.0, v6
	v_add_f32_e32 v8, 1.0, v8
	v_add_f32_e32 v7, 1.0, v7
	v_add_f32_e32 v9, 1.0, v9
	v_rcp_f32_e32 v11, v4
	v_add_f32_e32 v4, 1.0, v13
	v_rcp_f32_e32 v6, v6
	v_rcp_f32_e32 v8, v8
	v_rcp_f32_e32 v7, v7
	v_rcp_f32_e32 v9, v9
	v_rcp_f32_e32 v13, v4

.LBB0_453:
	s_andn2_b64 vcc, exec, s[0:1]
	s_cbranch_vccnz .LBB0_455
	v_pk_add_f32 v[10:11], v[48:49], v[108:109]
	v_pk_add_f32 v[6:7], v[46:47], v[106:107]
	v_pk_add_f32 v[8:9], v[50:51], v[102:103]
	v_pk_add_f32 v[12:13], v[52:53], v[104:105]
	v_mul_f32_e32 v6, 0xbfb8aa3b, v6
	v_mul_f32_e32 v8, 0xbfb8aa3b, v8
	v_mul_f32_e32 v7, 0xbfb8aa3b, v7
	v_mul_f32_e32 v9, 0xbfb8aa3b, v9
	v_mul_f32_e32 v10, 0xbfb8aa3b, v10
	v_mul_f32_e32 v12, 0xbfb8aa3b, v12
	v_mul_f32_e32 v11, 0xbfb8aa3b, v11
	v_mul_f32_e32 v13, 0xbfb8aa3b, v13
	v_exp_f32_e32 v6, v6
	v_exp_f32_e32 v8, v8
	v_exp_f32_e32 v7, v7
	v_exp_f32_e32 v9, v9
	v_exp_f32_e32 v10, v10
	v_exp_f32_e32 v12, v12
	v_exp_f32_e32 v11, v11
	v_exp_f32_e32 v13, v13
	v_add_f32_e32 v6, 1.0, v6
	v_add_f32_e32 v8, 1.0, v8
	v_add_f32_e32 v7, 1.0, v7
	v_add_f32_e32 v9, 1.0, v9
	v_add_f32_e32 v10, 1.0, v10
	v_add_f32_e32 v12, 1.0, v12
	v_add_f32_e32 v11, 1.0, v11
	v_add_f32_e32 v13, 1.0, v13
	v_rcp_f32_e32 v6, v6
	v_rcp_f32_e32 v8, v8
	v_rcp_f32_e32 v7, v7
	v_rcp_f32_e32 v9, v9
	v_rcp_f32_e32 v10, v10
	v_rcp_f32_e32 v12, v12
	v_rcp_f32_e32 v11, v11
	v_rcp_f32_e32 v13, v13

.LBB0_457:
	s_andn2_b64 vcc, exec, s[0:1]
	s_cbranch_vccnz .LBB0_459
	v_pk_add_f32 v[4:5], v[250:251], v[100:101]
	v_pk_add_f32 v[10:11], v[222:223], v[96:97]
	v_mul_f32_e32 v4, 0xbfb8aa3b, v4
	v_exp_f32_e32 v4, v4
	v_mul_f32_e32 v10, 0xbfb8aa3b, v10
	v_pk_add_f32 v[6:7], v[248:249], v[98:99]
	v_pk_add_f32 v[8:9], v[220:221], v[94:95]
	v_exp_f32_e32 v12, v10
	v_mul_f32_e32 v5, 0xbfb8aa3b, v5
	v_mul_f32_e32 v6, 0xbfb8aa3b, v6
	v_mul_f32_e32 v8, 0xbfb8aa3b, v8
	v_mul_f32_e32 v7, 0xbfb8aa3b, v7
	v_mul_f32_e32 v9, 0xbfb8aa3b, v9
	v_exp_f32_e32 v5, v5
	v_mul_f32_e32 v11, 0xbfb8aa3b, v11
	v_exp_f32_e32 v6, v6
	v_exp_f32_e32 v8, v8
	v_exp_f32_e32 v7, v7
	v_exp_f32_e32 v9, v9
	v_exp_f32_e32 v13, v11
	v_add_f32_e32 v4, 1.0, v4
	v_rcp_f32_e32 v10, v4
	v_add_f32_e32 v4, 1.0, v12
	v_rcp_f32_e32 v12, v4
	v_add_f32_e32 v4, 1.0, v5
	v_add_f32_e32 v6, 1.0, v6
	v_add_f32_e32 v8, 1.0, v8
	v_add_f32_e32 v7, 1.0, v7
	v_add_f32_e32 v9, 1.0, v9
	v_rcp_f32_e32 v11, v4
	v_add_f32_e32 v4, 1.0, v13
	v_rcp_f32_e32 v6, v6
	v_rcp_f32_e32 v8, v8
	v_rcp_f32_e32 v7, v7
	v_rcp_f32_e32 v9, v9
	v_rcp_f32_e32 v13, v4

.LBB0_461:
	s_andn2_b64 vcc, exec, s[0:1]
	s_cbranch_vccnz .LBB0_463
	v_pk_add_f32 v[10:11], v[48:49], v[92:93]
	v_pk_add_f32 v[6:7], v[46:47], v[90:91]
	v_pk_add_f32 v[8:9], v[50:51], v[86:87]
	v_pk_add_f32 v[12:13], v[52:53], v[88:89]
	v_mul_f32_e32 v6, 0xbfb8aa3b, v6
	v_mul_f32_e32 v8, 0xbfb8aa3b, v8
	v_mul_f32_e32 v7, 0xbfb8aa3b, v7
	v_mul_f32_e32 v9, 0xbfb8aa3b, v9
	v_mul_f32_e32 v10, 0xbfb8aa3b, v10
	v_mul_f32_e32 v12, 0xbfb8aa3b, v12
	v_mul_f32_e32 v11, 0xbfb8aa3b, v11
	v_mul_f32_e32 v13, 0xbfb8aa3b, v13
	v_exp_f32_e32 v6, v6
	v_exp_f32_e32 v8, v8
	v_exp_f32_e32 v7, v7
	v_exp_f32_e32 v9, v9
	v_exp_f32_e32 v10, v10
	v_exp_f32_e32 v12, v12
	v_exp_f32_e32 v11, v11
	v_exp_f32_e32 v13, v13
	v_add_f32_e32 v6, 1.0, v6
	v_add_f32_e32 v8, 1.0, v8
	v_add_f32_e32 v7, 1.0, v7
	v_add_f32_e32 v9, 1.0, v9
	v_add_f32_e32 v10, 1.0, v10
	v_add_f32_e32 v12, 1.0, v12
	v_add_f32_e32 v11, 1.0, v11
	v_add_f32_e32 v13, 1.0, v13
	v_rcp_f32_e32 v6, v6
	v_rcp_f32_e32 v8, v8
	v_rcp_f32_e32 v7, v7
	v_rcp_f32_e32 v9, v9
	v_rcp_f32_e32 v10, v10
	v_rcp_f32_e32 v12, v12
	v_rcp_f32_e32 v11, v11
	v_rcp_f32_e32 v13, v13

.LBB0_465:
	s_andn2_b64 vcc, exec, s[0:1]
	s_cbranch_vccnz .LBB0_467
	v_pk_add_f32 v[4:5], v[250:251], v[84:85]
	v_pk_add_f32 v[10:11], v[222:223], v[80:81]
	v_mul_f32_e32 v4, 0xbfb8aa3b, v4
	v_exp_f32_e32 v4, v4
	v_mul_f32_e32 v10, 0xbfb8aa3b, v10
	v_pk_add_f32 v[6:7], v[248:249], v[82:83]
	v_pk_add_f32 v[8:9], v[220:221], v[78:79]
	v_exp_f32_e32 v12, v10
	v_mul_f32_e32 v5, 0xbfb8aa3b, v5
	v_mul_f32_e32 v6, 0xbfb8aa3b, v6
	v_mul_f32_e32 v8, 0xbfb8aa3b, v8
	v_mul_f32_e32 v7, 0xbfb8aa3b, v7
	v_mul_f32_e32 v9, 0xbfb8aa3b, v9
	v_exp_f32_e32 v5, v5
	v_mul_f32_e32 v11, 0xbfb8aa3b, v11
	v_exp_f32_e32 v6, v6
	v_exp_f32_e32 v8, v8
	v_exp_f32_e32 v7, v7
	v_exp_f32_e32 v9, v9
	v_exp_f32_e32 v13, v11
	v_add_f32_e32 v4, 1.0, v4
	v_rcp_f32_e32 v10, v4
	v_add_f32_e32 v4, 1.0, v12
	v_rcp_f32_e32 v12, v4
	v_add_f32_e32 v4, 1.0, v5
	v_add_f32_e32 v6, 1.0, v6
	v_add_f32_e32 v8, 1.0, v8
	v_add_f32_e32 v7, 1.0, v7
	v_add_f32_e32 v9, 1.0, v9
	v_rcp_f32_e32 v11, v4
	v_add_f32_e32 v4, 1.0, v13
	v_rcp_f32_e32 v6, v6
	v_rcp_f32_e32 v8, v8
	v_rcp_f32_e32 v7, v7
	v_rcp_f32_e32 v9, v9
	v_rcp_f32_e32 v13, v4

.LBB0_469:
	s_andn2_b64 vcc, exec, s[0:1]
	s_cbranch_vccnz .LBB0_471
	v_pk_add_f32 v[10:11], v[48:49], v[76:77]
	v_pk_add_f32 v[6:7], v[46:47], v[74:75]
	v_pk_add_f32 v[8:9], v[50:51], v[70:71]
	v_pk_add_f32 v[12:13], v[52:53], v[72:73]
	v_mul_f32_e32 v6, 0xbfb8aa3b, v6
	v_mul_f32_e32 v8, 0xbfb8aa3b, v8
	v_mul_f32_e32 v7, 0xbfb8aa3b, v7
	v_mul_f32_e32 v9, 0xbfb8aa3b, v9
	v_mul_f32_e32 v10, 0xbfb8aa3b, v10
	v_mul_f32_e32 v12, 0xbfb8aa3b, v12
	v_mul_f32_e32 v11, 0xbfb8aa3b, v11
	v_mul_f32_e32 v13, 0xbfb8aa3b, v13
	v_exp_f32_e32 v6, v6
	v_exp_f32_e32 v8, v8
	v_exp_f32_e32 v7, v7
	v_exp_f32_e32 v9, v9
	v_exp_f32_e32 v10, v10
	v_exp_f32_e32 v12, v12
	v_exp_f32_e32 v11, v11
	v_exp_f32_e32 v13, v13
	v_add_f32_e32 v6, 1.0, v6
	v_add_f32_e32 v8, 1.0, v8
	v_add_f32_e32 v7, 1.0, v7
	v_add_f32_e32 v9, 1.0, v9
	v_add_f32_e32 v10, 1.0, v10
	v_add_f32_e32 v12, 1.0, v12
	v_add_f32_e32 v11, 1.0, v11
	v_add_f32_e32 v13, 1.0, v13
	v_rcp_f32_e32 v6, v6
	v_rcp_f32_e32 v8, v8
	v_rcp_f32_e32 v7, v7
	v_rcp_f32_e32 v9, v9
	v_rcp_f32_e32 v10, v10
	v_rcp_f32_e32 v12, v12
	v_rcp_f32_e32 v11, v11
	v_rcp_f32_e32 v13, v13

.LBB0_473:
	s_andn2_b64 vcc, exec, s[0:1]
	s_cbranch_vccnz .LBB0_475
	v_pk_add_f32 v[4:5], v[250:251], v[68:69]
	v_pk_add_f32 v[10:11], v[222:223], v[64:65]
	v_mul_f32_e32 v4, 0xbfb8aa3b, v4
	v_exp_f32_e32 v4, v4
	v_mul_f32_e32 v10, 0xbfb8aa3b, v10
	v_pk_add_f32 v[6:7], v[248:249], v[66:67]
	v_pk_add_f32 v[8:9], v[220:221], v[62:63]
	v_exp_f32_e32 v12, v10
	v_mul_f32_e32 v5, 0xbfb8aa3b, v5
	v_mul_f32_e32 v6, 0xbfb8aa3b, v6
	v_mul_f32_e32 v8, 0xbfb8aa3b, v8
	v_mul_f32_e32 v7, 0xbfb8aa3b, v7
	v_mul_f32_e32 v9, 0xbfb8aa3b, v9
	v_exp_f32_e32 v5, v5
	v_mul_f32_e32 v11, 0xbfb8aa3b, v11
	v_exp_f32_e32 v6, v6
	v_exp_f32_e32 v8, v8
	v_exp_f32_e32 v7, v7
	v_exp_f32_e32 v9, v9
	v_exp_f32_e32 v13, v11
	v_add_f32_e32 v4, 1.0, v4
	v_rcp_f32_e32 v10, v4
	v_add_f32_e32 v4, 1.0, v12
	v_rcp_f32_e32 v12, v4
	v_add_f32_e32 v4, 1.0, v5
	v_add_f32_e32 v6, 1.0, v6
	v_add_f32_e32 v8, 1.0, v8
	v_add_f32_e32 v7, 1.0, v7
	v_add_f32_e32 v9, 1.0, v9
	v_rcp_f32_e32 v11, v4
	v_add_f32_e32 v4, 1.0, v13
	v_rcp_f32_e32 v6, v6
	v_rcp_f32_e32 v8, v8
	v_rcp_f32_e32 v7, v7
	v_rcp_f32_e32 v9, v9
	v_rcp_f32_e32 v13, v4

.LBB0_477:
	s_andn2_b64 vcc, exec, s[0:1]
	s_cbranch_vccnz .LBB0_479
	v_pk_add_f32 v[2:3], v[48:49], v[60:61]
	v_pk_add_f32 v[10:11], v[52:53], v[56:57]
	v_mul_f32_e32 v2, 0xbfb8aa3b, v2
	v_exp_f32_e32 v2, v2
	v_mul_f32_e32 v10, 0xbfb8aa3b, v10
	v_pk_add_f32 v[6:7], v[46:47], v[58:59]
	v_pk_add_f32 v[8:9], v[50:51], v[54:55]
	v_exp_f32_e32 v12, v10
	v_mul_f32_e32 v3, 0xbfb8aa3b, v3
	v_mul_f32_e32 v6, 0xbfb8aa3b, v6
	v_mul_f32_e32 v8, 0xbfb8aa3b, v8
	v_mul_f32_e32 v7, 0xbfb8aa3b, v7
	v_mul_f32_e32 v9, 0xbfb8aa3b, v9
	v_exp_f32_e32 v3, v3
	v_mul_f32_e32 v11, 0xbfb8aa3b, v11
	v_exp_f32_e32 v6, v6
	v_exp_f32_e32 v8, v8
	v_exp_f32_e32 v7, v7
	v_exp_f32_e32 v9, v9
	v_exp_f32_e32 v13, v11
	v_add_f32_e32 v2, 1.0, v2
	v_rcp_f32_e32 v10, v2
	v_add_f32_e32 v2, 1.0, v12
	v_rcp_f32_e32 v12, v2
	v_add_f32_e32 v2, 1.0, v3
	v_add_f32_e32 v6, 1.0, v6
	v_add_f32_e32 v8, 1.0, v8
	v_add_f32_e32 v7, 1.0, v7
	v_add_f32_e32 v9, 1.0, v9
	v_rcp_f32_e32 v11, v2
	v_add_f32_e32 v2, 1.0, v13
	v_rcp_f32_e32 v6, v6
	v_rcp_f32_e32 v8, v8
	v_rcp_f32_e32 v7, v7
	v_rcp_f32_e32 v9, v9
	v_rcp_f32_e32 v13, v2
